# N1 (layers 1,3): per-token expert index / rank / residual row loads issued one token ahead into spare VGPRs (one exposed memory round trip per token instead of two), on top of previous stack
# baseline (speedup 1.0000x reference)
; __device__ __forceinline__ void n1_phase(const Args& a, int layer, bool final_only, const int wv, const bool dry = false) {
;     ...
;     for (int run = F.bid * 8 + F.wave; run < NTOK / 16; run += F.G * 8) {
;         const int tok0 = run * 16, b = tok0 >> 12;
;         f32x4 g2s[4], ma[4], mb[4];
;         if (combine) { const float* g2 = mod + ((size_t)(layer - 1) * NBATCH + b) * 6144 + 5 * DM;
; #pragma unroll
;             for (int j = 0; j < 4; ++j) g2s[j] = *(const f32x4*)(g2 + 4 * F.lane + 256 * j) * (1.f / FP8_YSC); }
;         if (!final_only) { const float* sh = mod + ((size_t)layer * NBATCH + b) * 6144; const float* sc = sh + DM;
; #pragma unroll
;             for (int j = 0; j < 4; ++j) { const int c0 = 4 * F.lane + 256 * j; ma[j] = *(const f32x4*)(gmix + c0) * (*(const f32x4*)(sc + c0) + 1.f); mb[j] = *(const f32x4*)(sh + c0); } }
; #pragma unroll 1
;         for (int i = 0; i < 16; ++i) {
;             const int tok = tok0 + i;
;             f32x4 v[4];
;             if (layer == 0) ld_row16(a.x + (size_t)tok * DM, F.lane, v);
;             else {
; #pragma unroll
;                 for (int j = 0; j < 4; ++j) { const u32x2 w = *(const u32x2*)(XB + (size_t)tok * DM + 4 * F.lane + 256 * j); v[j] = (f32x4){bf_lo(w.x), bf_hi(w.x), bf_lo(w.y), bf_hi(w.y)}; } }
;             if (combine) {
;                 f32x4 ysum[4];
; #pragma unroll
;                 for (int j = 0; j < 4; ++j) ysum[j] = (f32x4){0.f, 0.f, 0.f, 0.f};
; #pragma unroll
;                 for (int k = 0; k < 4; ++k) { const int e = toke[tok * 4 + k], r = tokr[tok * 4 + k]; const size_t slot = (size_t)ps[e] + r;
.LBB0_1601:
	s_ashr_i32 s7, s6, 31
	s_lshl_b64 s[2:3], s[6:7], 10
	s_lshl_b64 s[16:17], s[6:7], 11
	s_ashr_i32 s7, s20, 8
	s_mul_hi_i32 s43, s7, 0x6000
	s_mulk_i32 s7, 0x6000
	s_add_u32 s44, s21, s7
	s_addc_u32 s45, s22, s43
	v_lshl_add_u64 v[0:1], s[44:45], 0, v[30:31]
	v_lshl_add_u64 v[2:3], v[0:1], 0, s[8:9]
	v_add_co_u32_e32 v0, vcc, s38, v0
	s_add_u32 s46, s44, 0x30000
	s_nop 0
	v_addc_co_u32_e32 v1, vcc, 0, v1, vcc
	global_load_dwordx4 v[38:41], v[0:1], off
	global_load_dwordx4 v[42:45], v[2:3], off offset:1024
	global_load_dwordx4 v[46:49], v[2:3], off offset:2048
	global_load_dwordx4 v[50:53], v[2:3], off offset:3072
	s_addc_u32 s47, s45, 0
	s_add_u32 s44, s44, 0x31000
	s_addc_u32 s45, s45, 0
	global_load_dwordx4 v[54:57], v30, s[44:45]
	global_load_dwordx4 v[58:61], v77, s[44:45]
	global_load_dwordx4 v[62:65], v78, s[44:45]
	global_load_dwordx4 v[66:69], v79, s[44:45]
	global_load_dwordx4 v[82:85], v[20:21], off
	global_load_dwordx4 v[86:89], v[22:23], off
	global_load_dwordx4 v[90:93], v[24:25], off
	global_load_dwordx4 v[0:3], v30, s[46:47]
	global_load_dwordx4 v[94:97], v[26:27], off
	global_load_dwordx4 v[4:7], v77, s[46:47]
	global_load_dwordx4 v[8:11], v78, s[46:47]
	global_load_dwordx4 v[12:15], v79, s[46:47]
	v_mov_b32_e32 v33, s3
	v_or_b32_e32 v32, s2, v16
	v_mov_b32_e32 v35, s17
	v_or_b32_e32 v34, s16, v28
	s_mov_b32 s7, 0
	s_waitcnt vmcnt(11)
	v_pk_add_f32 v[54:55], v[54:55], 1.0 op_sel_hi:[1,0]
	s_waitcnt vmcnt(10)
	v_pk_add_f32 v[58:59], v[58:59], 1.0 op_sel_hi:[1,0]
	s_waitcnt vmcnt(9)
	v_pk_add_f32 v[62:63], v[62:63], 1.0 op_sel_hi:[1,0]
	s_waitcnt vmcnt(8)
	v_pk_add_f32 v[66:67], v[66:67], 1.0 op_sel_hi:[1,0]
	v_pk_mul_f32 v[36:37], v[40:41], s[10:11] op_sel_hi:[1,0]
	v_pk_mul_f32 v[40:41], v[44:45], s[10:11] op_sel_hi:[1,0]
	v_pk_mul_f32 v[44:45], v[48:49], s[10:11] op_sel_hi:[1,0]
	v_pk_mul_f32 v[48:49], v[52:53], s[10:11] op_sel_hi:[1,0]
	v_pk_add_f32 v[52:53], v[56:57], 1.0 op_sel_hi:[1,0]
	v_pk_add_f32 v[56:57], v[60:61], 1.0 op_sel_hi:[1,0]
	v_pk_add_f32 v[60:61], v[64:65], 1.0 op_sel_hi:[1,0]
	v_pk_add_f32 v[64:65], v[68:69], 1.0 op_sel_hi:[1,0]
	v_pk_mul_f32 v[38:39], v[38:39], s[10:11] op_sel_hi:[1,0]
	v_pk_mul_f32 v[42:43], v[42:43], s[10:11] op_sel_hi:[1,0]
	v_pk_mul_f32 v[46:47], v[46:47], s[10:11] op_sel_hi:[1,0]
	v_pk_mul_f32 v[50:51], v[50:51], s[10:11] op_sel_hi:[1,0]
	s_waitcnt vmcnt(7)
	v_pk_mul_f32 v[52:53], v[84:85], v[52:53]
	v_pk_mul_f32 v[54:55], v[82:83], v[54:55]
	s_waitcnt vmcnt(6)
	v_pk_mul_f32 v[56:57], v[88:89], v[56:57]
	v_pk_mul_f32 v[58:59], v[86:87], v[58:59]
	s_waitcnt vmcnt(5)
	v_pk_mul_f32 v[60:61], v[92:93], v[60:61]
	v_pk_mul_f32 v[62:63], v[90:91], v[62:63]
	s_waitcnt vmcnt(3)
	v_pk_mul_f32 v[64:65], v[96:97], v[64:65]
	v_pk_mul_f32 v[66:67], v[94:95], v[66:67]
	v_lshl_add_u64 v[166:167], s[4:5], 0, v[34:35]
	s_add_i32 s16, s33, s7
	s_ashr_i32 s17, s16, 31
	s_lshl_b64 s[2:3], s[16:17], 2
	v_add_co_u32_e32 v166, vcc, 0xaf200000, v166
	s_add_u32 s44, s23, s2
	s_nop 0
	v_addc_co_u32_e32 v167, vcc, 0, v167, vcc
	s_addc_u32 s45, s24, s3
	global_load_dwordx2 v[170:171], v[166:167], off
	global_load_dwordx2 v[172:173], v[166:167], off offset:512
	global_load_dwordx2 v[174:175], v[166:167], off offset:1024
	global_load_dwordx2 v[176:177], v[166:167], off offset:1536
	global_load_dwordx4 v[178:181], v17, s[44:45]
	s_add_u32 s2, s25, s2
	s_addc_u32 s3, s26, s3
	s_add_i32 s16, s16, 1
	s_ashr_i32 s17, s16, 31
	global_load_dword v182, v17, s[2:3]
	s_lshl_b64 s[2:3], s[16:17], 2
	s_add_u32 s2, s25, s2
	s_addc_u32 s3, s26, s3
	global_load_dwordx3 v[184:186], v17, s[2:3]
	s_waitcnt vmcnt(0)
.LBB0_1602:
	v_mov_b64_e32 v[90:91], v[170:171]
	v_mov_b64_e32 v[92:93], v[172:173]
	v_mov_b64_e32 v[94:95], v[174:175]
	v_mov_b64_e32 v[96:97], v[176:177]
	v_mov_b64_e32 v[82:83], v[178:179]
	v_mov_b64_e32 v[84:85], v[180:181]
	v_mov_b32_e32 v98, v182
	v_mov_b32_e32 v86, v184
	v_mov_b32_e32 v87, v185
	v_mov_b32_e32 v88, v186
	v_lshl_add_u64 v[70:71], s[4:5], 0, v[32:33]
	s_add_i32 s16, s33, s7
	v_add_co_u32_e64 v70, s[2:3], s42, v70
	s_ashr_i32 s17, s16, 31
	s_nop 0
	v_addc_co_u32_e64 v71, s[2:3], 0, v71, s[2:3]
	v_lshl_add_u64 v[68:69], s[4:5], 0, v[34:35]
	s_lshl_b64 s[2:3], s[16:17], 2
	v_add_co_u32_e32 v68, vcc, 0xaf200000, v68
	s_add_u32 s44, s23, s2
	s_nop 0
	v_addc_co_u32_e32 v69, vcc, 0, v69, vcc
	s_addc_u32 s45, s24, s3
	s_add_u32 s2, s25, s2
	s_addc_u32 s3, s26, s3
	s_add_i32 s16, s16, 1
	s_ashr_i32 s17, s16, 31
	s_lshl_b64 s[2:3], s[16:17], 2
	s_add_u32 s2, s25, s2
	s_addc_u32 s3, s26, s3
	v_mov_b32_e32 v162, 0
	v_mov_b32_e32 v163, 0
	v_mov_b32_e32 v164, 0
	v_mov_b32_e32 v165, 0
	s_add_i32 s7, s7, 4
	v_lshl_add_u64 v[32:33], v[32:33], 0, s[12:13]
	v_lshl_add_u64 v[34:35], v[34:35], 0, s[14:15]
	s_cmp_lt_u32 s7, 64
	s_cbranch_scc0 .Ln1pf0_skip
	v_lshl_add_u64 v[166:167], s[4:5], 0, v[34:35]
	s_add_i32 s16, s33, s7
	s_ashr_i32 s17, s16, 31
	s_lshl_b64 s[2:3], s[16:17], 2
	v_add_co_u32_e32 v166, vcc, 0xaf200000, v166
	s_add_u32 s44, s23, s2
	s_nop 0
	v_addc_co_u32_e32 v167, vcc, 0, v167, vcc
	s_addc_u32 s45, s24, s3
	global_load_dwordx2 v[170:171], v[166:167], off
	global_load_dwordx2 v[172:173], v[166:167], off offset:512
	global_load_dwordx2 v[174:175], v[166:167], off offset:1024
	global_load_dwordx2 v[176:177], v[166:167], off offset:1536
	global_load_dwordx4 v[178:181], v17, s[44:45]
	s_add_u32 s2, s25, s2
	s_addc_u32 s3, s26, s3
	s_add_i32 s16, s16, 1
	s_ashr_i32 s17, s16, 31
	global_load_dword v182, v17, s[2:3]
	s_lshl_b64 s[2:3], s[16:17], 2
	s_add_u32 s2, s25, s2
	s_addc_u32 s3, s26, s3
	global_load_dwordx3 v[184:186], v17, s[2:3]
; __device__ __forceinline__ void n1_phase(const Args& a, int layer, bool final_only, const int wv, const bool dry = false) {
;     ...
;             if (combine) {
;                 f32x4 ysum[4];
; #pragma unroll
;                 for (int j = 0; j < 4; ++j) ysum[j] = (f32x4){0.f, 0.f, 0.f, 0.f};
; #pragma unroll
;                 for (int k = 0; k < 4; ++k) { const int e = toke[tok * 4 + k], r = tokr[tok * 4 + k]; const size_t slot = (size_t)ps[e] + r;
;                     const unsigned char* yr = Y + slot * DM + 4 * F.lane;
; #pragma unroll
;                     for (int j = 0; j < 4; ++j) { const int w = *(const int*)(yr + 256 * j); const f32x2 lo = __builtin_amdgcn_cvt_pk_f32_fp8(w, false), hi = __builtin_amdgcn_cvt_pk_f32_fp8(w, true);
;                         ysum[j][0] += lo[0]; ysum[j][1] += lo[1]; ysum[j][2] += hi[0]; ysum[j][3] += hi[1]; } }
.Ln1pf0_skip:
	s_cmp_eq_u32 s7, 64
	v_lshlrev_b32_e32 v100, 16, v90
	v_and_b32_e32 v101, 0xffff0000, v90
	v_lshlrev_b32_e32 v102, 16, v92
	v_and_b32_e32 v103, 0xffff0000, v92
	v_lshlrev_b32_e32 v82, 2, v82
	v_lshlrev_b32_e32 v83, 2, v83
	v_lshlrev_b32_e32 v84, 2, v84
	v_lshlrev_b32_e32 v85, 2, v85
	v_add_u32_e32 v82, s39, v82
	v_add_u32_e32 v83, s39, v83
	v_add_u32_e32 v89, s39, v84
	v_add_u32_e32 v85, s39, v85
	ds_read_b32 v82, v82
	ds_read_b32 v84, v83
	ds_read_b32 v108, v89
	ds_read_b32 v110, v85
	v_ashrrev_i32_e32 v99, 31, v98
	s_waitcnt lgkmcnt(3)
	v_ashrrev_i32_e32 v83, 31, v82
	v_ashrrev_i32_e32 v113, 31, v86
	v_mov_b32_e32 v112, v86
	v_ashrrev_i32_e32 v115, 31, v87
	v_mov_b32_e32 v114, v87
	v_ashrrev_i32_e32 v87, 31, v88
	v_mov_b32_e32 v86, v88
	s_waitcnt lgkmcnt(2)
	v_ashrrev_i32_e32 v85, 31, v84
	s_waitcnt lgkmcnt(1)
	v_ashrrev_i32_e32 v109, 31, v108
	s_waitcnt lgkmcnt(0)
	v_ashrrev_i32_e32 v111, 31, v110
	v_lshl_add_u64 v[82:83], v[82:83], 0, v[98:99]
	v_lshl_add_u64 v[84:85], v[84:85], 0, v[112:113]
	v_lshl_add_u64 v[88:89], v[108:109], 0, v[114:115]
	v_lshl_add_u64 v[86:87], v[110:111], 0, v[86:87]
	v_lshlrev_b64 v[82:83], 10, v[82:83]
	v_lshlrev_b64 v[84:85], 10, v[84:85]
	v_lshlrev_b64 v[88:89], 10, v[88:89]
	v_lshlrev_b64 v[86:87], 10, v[86:87]
	v_lshl_add_u64 v[82:83], v[18:19], 0, v[82:83]
	v_lshl_add_u64 v[84:85], v[18:19], 0, v[84:85]
	v_lshl_add_u64 v[88:89], v[18:19], 0, v[88:89]
	v_lshl_add_u64 v[86:87], v[18:19], 0, v[86:87]
	global_load_dword v98, v[82:83], off
	global_load_dword v99, v[82:83], off offset:256
	global_load_dword v108, v[82:83], off offset:512
	global_load_dword v112, v[82:83], off offset:768
	global_load_dword v116, v[84:85], off
	global_load_dword v120, v[84:85], off offset:256
	global_load_dword v124, v[84:85], off offset:512
	global_load_dword v128, v[84:85], off offset:768
	global_load_dword v132, v[88:89], off
	global_load_dword v136, v[88:89], off offset:256
	global_load_dword v140, v[88:89], off offset:512
	global_load_dword v144, v[88:89], off offset:768
	global_load_dword v148, v[86:87], off
	global_load_dword v152, v[86:87], off offset:256
	global_load_dword v156, v[86:87], off offset:512
	global_load_dword v160, v[86:87], off offset:768
	v_lshlrev_b32_e32 v90, 16, v91
	v_and_b32_e32 v91, 0xffff0000, v91
	v_lshlrev_b32_e32 v92, 16, v93
	v_and_b32_e32 v93, 0xffff0000, v93
	v_lshlrev_b32_e32 v104, 16, v94
	v_and_b32_e32 v105, 0xffff0000, v94
	v_lshlrev_b32_e32 v94, 16, v95
	v_and_b32_e32 v95, 0xffff0000, v95
	v_lshlrev_b32_e32 v106, 16, v96
	v_and_b32_e32 v107, 0xffff0000, v96
	v_lshlrev_b32_e32 v96, 16, v97
	v_and_b32_e32 v97, 0xffff0000, v97
	s_waitcnt vmcnt(15)
	v_cvt_pk_f32_fp8_e32 v[82:83], v98
	s_waitcnt vmcnt(14)
	v_cvt_pk_f32_fp8_e32 v[86:87], v99
	v_cvt_pk_f32_fp8_sdwa v[84:85], v98 src0_sel:WORD_1
	v_cvt_pk_f32_fp8_sdwa v[88:89], v99 src0_sel:WORD_1
	s_waitcnt vmcnt(13)
	v_cvt_pk_f32_fp8_e32 v[98:99], v108
	v_cvt_pk_f32_fp8_sdwa v[108:109], v108 src0_sel:WORD_1
	s_waitcnt vmcnt(12)
	v_cvt_pk_f32_fp8_e32 v[110:111], v112
	v_cvt_pk_f32_fp8_sdwa v[112:113], v112 src0_sel:WORD_1
	s_waitcnt vmcnt(11)
	v_cvt_pk_f32_fp8_e32 v[114:115], v116
	s_waitcnt vmcnt(10)
	v_cvt_pk_f32_fp8_e32 v[118:119], v120
	v_cvt_pk_f32_fp8_sdwa v[116:117], v116 src0_sel:WORD_1
	v_cvt_pk_f32_fp8_sdwa v[120:121], v120 src0_sel:WORD_1
	s_waitcnt vmcnt(9)
	v_cvt_pk_f32_fp8_e32 v[122:123], v124
	v_cvt_pk_f32_fp8_sdwa v[124:125], v124 src0_sel:WORD_1
	s_waitcnt vmcnt(8)
	v_cvt_pk_f32_fp8_e32 v[126:127], v128
	v_cvt_pk_f32_fp8_sdwa v[128:129], v128 src0_sel:WORD_1
	s_waitcnt vmcnt(7)
	v_cvt_pk_f32_fp8_e32 v[130:131], v132
	s_waitcnt vmcnt(6)
	v_cvt_pk_f32_fp8_e32 v[134:135], v136
	v_cvt_pk_f32_fp8_sdwa v[132:133], v132 src0_sel:WORD_1
	v_cvt_pk_f32_fp8_sdwa v[136:137], v136 src0_sel:WORD_1
	s_waitcnt vmcnt(5)
	v_cvt_pk_f32_fp8_e32 v[138:139], v140
	v_cvt_pk_f32_fp8_sdwa v[140:141], v140 src0_sel:WORD_1
	s_waitcnt vmcnt(4)
	v_cvt_pk_f32_fp8_e32 v[142:143], v144
	v_cvt_pk_f32_fp8_sdwa v[144:145], v144 src0_sel:WORD_1
	s_waitcnt vmcnt(3)
	v_cvt_pk_f32_fp8_e32 v[146:147], v148
	s_waitcnt vmcnt(2)
	v_cvt_pk_f32_fp8_e32 v[150:151], v152
	v_cvt_pk_f32_fp8_sdwa v[148:149], v148 src0_sel:WORD_1
	v_cvt_pk_f32_fp8_sdwa v[152:153], v152 src0_sel:WORD_1
	s_waitcnt vmcnt(1)
	v_cvt_pk_f32_fp8_e32 v[154:155], v156
	v_cvt_pk_f32_fp8_sdwa v[156:157], v156 src0_sel:WORD_1
	s_waitcnt vmcnt(0)
; __device__ __forceinline__ unsigned cvt_pk_bf16(float lo, float hi) { unsigned r; asm volatile("v_cvt_pk_bf16_f32 %0, %1, %2" : "=v"(r) : "v"(lo), "v"(hi)); return r; }
; __device__ __forceinline__ unsigned pk4_fp8c(float a, float b, float c, float d) { return pk4_fp8(__builtin_amdgcn_fmed3f(a, -448.f, 448.f), __builtin_amdgcn_fmed3f(b, -448.f, 448.f), __builtin_amdgcn_fmed3f(c, -448.f, 448.f), __builtin_amdgcn_fmed3f(d, -448.f, 448.f)); }
; __device__ __forceinline__ void n1_phase(const Args& a, int layer, bool final_only, const int wv, const bool dry = false) {
;     ...
;                         ysum[j][0] += lo[0]; ysum[j][1] += lo[1]; ysum[j][2] += hi[0]; ysum[j][3] += hi[1]; } }
; #pragma unroll
;                 for (int j = 0; j < 4; ++j) { v[j] = v[j] + g2s[j] * ysum[j];
;                     if (final_only) *(f32x4*)(a.out + (size_t)tok * DM + 4 * F.lane + 256 * j) = v[j];
;                     else { u32x2 o; o.x = cvt_pk_bf16(v[j][0], v[j][1]); o.y = cvt_pk_bf16(v[j][2], v[j][3]); *(u32x2*)((dry ? (bf16_t*)(ws + WS_ACT) : XB) + (size_t)tok * DM + 4 * F.lane + 256 * j) = o; } }
;             }
;             if (final_only) continue;
;             float ss = 0.f;
; #pragma unroll
;             for (int j = 0; j < 4; ++j) ss += v[j][0] * v[j][0] + v[j][1] * v[j][1] + v[j][2] * v[j][2] + v[j][3] * v[j][3];
;             const float inv = rsqrtf(wave_sum(ss, F.lane) * (1.f / DM) + EPS);
; #pragma unroll
;             for (int j = 0; j < 4; ++j) { const int c0 = 4 * F.lane + 256 * j;
;                 const f32x4 h = v[j] * inv * ma[j] + mb[j];
;                 if (layer & 1) *(unsigned*)((unsigned char*)HM + (size_t)tok * DM + c0) = pg8::pk4_fp8c(h[0] * FP8_HSC, h[1] * FP8_HSC, h[2] * FP8_HSC, h[3] * FP8_HSC);
;                 else { u32x2 o; o.x = cvt_pk_bf16(h[0], h[1]); o.y = cvt_pk_bf16(h[2], h[3]); *(u32x2*)(HM + (size_t)tok * DM + c0) = o; } }
	v_cvt_pk_f32_fp8_e32 v[158:159], v160
	v_cvt_pk_f32_fp8_sdwa v[160:161], v160 src0_sel:WORD_1
	v_pk_add_f32 v[82:83], v[82:83], 0 op_sel_hi:[1,0]
	v_pk_add_f32 v[86:87], v[86:87], 0 op_sel_hi:[1,0]
	v_pk_add_f32 v[84:85], v[84:85], 0 op_sel_hi:[1,0]
	v_pk_add_f32 v[88:89], v[88:89], 0 op_sel_hi:[1,0]
	v_pk_add_f32 v[108:109], v[108:109], 0 op_sel_hi:[1,0]
	v_pk_add_f32 v[98:99], v[98:99], 0 op_sel_hi:[1,0]
	v_pk_add_f32 v[112:113], v[112:113], 0 op_sel_hi:[1,0]
	v_pk_add_f32 v[110:111], v[110:111], 0 op_sel_hi:[1,0]
	v_pk_add_f32 v[82:83], v[82:83], v[114:115]
	v_pk_add_f32 v[86:87], v[86:87], v[118:119]
	v_pk_add_f32 v[84:85], v[84:85], v[116:117]
	v_pk_add_f32 v[88:89], v[88:89], v[120:121]
	v_pk_add_f32 v[98:99], v[98:99], v[122:123]
	v_pk_add_f32 v[108:109], v[108:109], v[124:125]
	v_pk_add_f32 v[110:111], v[110:111], v[126:127]
	v_pk_add_f32 v[112:113], v[112:113], v[128:129]
	v_pk_add_f32 v[82:83], v[82:83], v[130:131]
	v_pk_add_f32 v[86:87], v[86:87], v[134:135]
	v_pk_add_f32 v[84:85], v[84:85], v[132:133]
	v_pk_add_f32 v[88:89], v[88:89], v[136:137]
	v_pk_add_f32 v[108:109], v[108:109], v[140:141]
	v_pk_add_f32 v[98:99], v[98:99], v[138:139]
	v_pk_add_f32 v[112:113], v[112:113], v[144:145]
	v_pk_add_f32 v[110:111], v[110:111], v[142:143]
	v_pk_add_f32 v[82:83], v[82:83], v[146:147]
	v_pk_add_f32 v[86:87], v[86:87], v[150:151]
	v_pk_add_f32 v[84:85], v[84:85], v[148:149]
	v_pk_add_f32 v[88:89], v[88:89], v[152:153]
	v_pk_add_f32 v[98:99], v[98:99], v[154:155]
	v_pk_add_f32 v[108:109], v[108:109], v[156:157]
	v_pk_add_f32 v[110:111], v[110:111], v[158:159]
	v_pk_add_f32 v[112:113], v[112:113], v[160:161]
	v_pk_fma_f32 v[82:83], v[38:39], v[82:83], v[100:101]
	v_pk_fma_f32 v[86:87], v[42:43], v[86:87], v[102:103]
	v_pk_fma_f32 v[84:85], v[36:37], v[84:85], v[90:91]
	v_pk_fma_f32 v[88:89], v[40:41], v[88:89], v[92:93]
	v_pk_fma_f32 v[90:91], v[44:45], v[108:109], v[94:95]
	v_pk_fma_f32 v[92:93], v[46:47], v[98:99], v[104:105]
	v_pk_fma_f32 v[94:95], v[48:49], v[112:113], v[96:97]
	v_pk_fma_f32 v[96:97], v[50:51], v[110:111], v[106:107]
	v_mov_b32_e32 v102, v83
	v_mov_b32_e32 v103, v87
	v_cvt_pk_bf16_f32 v98, v82, v83
	v_cvt_pk_bf16_f32 v99, v84, v85
	v_mov_b32_e32 v100, v82
	v_mov_b32_e32 v101, v86
	v_mov_b32_e32 v110, v93
	v_mov_b32_e32 v111, v97
	v_pk_mul_f32 v[102:103], v[102:103], v[102:103]
	v_mov_b32_e32 v104, v84
	v_mov_b32_e32 v105, v88
	v_mov_b32_e32 v108, v92
	v_mov_b32_e32 v109, v96
	global_store_dwordx2 v[68:69], v[98:99], off
	v_cvt_pk_bf16_f32 v98, v86, v87
	v_cvt_pk_bf16_f32 v99, v88, v89
	v_pk_mul_f32 v[110:111], v[110:111], v[110:111]
	v_pk_fma_f32 v[100:101], v[100:101], v[100:101], v[102:103]
	v_mov_b32_e32 v106, v85
	v_mov_b32_e32 v107, v89
	v_mov_b32_e32 v112, v90
	v_mov_b32_e32 v113, v94
	global_store_dwordx2 v[68:69], v[98:99], off offset:512
	v_cvt_pk_bf16_f32 v98, v92, v93
	v_cvt_pk_bf16_f32 v99, v90, v91
	v_pk_fma_f32 v[102:103], v[108:109], v[108:109], v[110:111]
	v_pk_fma_f32 v[100:101], v[104:105], v[104:105], v[100:101]
	v_mov_b32_e32 v114, v91
	v_mov_b32_e32 v115, v95
	global_store_dwordx2 v[68:69], v[98:99], off offset:1024
	v_cvt_pk_bf16_f32 v98, v96, v97
	v_cvt_pk_bf16_f32 v99, v94, v95
	v_pk_fma_f32 v[102:103], v[112:113], v[112:113], v[102:103]
	global_store_dwordx2 v[68:69], v[98:99], off offset:1536
	v_pk_fma_f32 v[68:69], v[106:107], v[106:107], v[100:101]
	v_pk_fma_f32 v[98:99], v[114:115], v[114:115], v[102:103]
	v_add_f32_e32 v68, v68, v69
	v_add_f32_e32 v68, v68, v98
	v_add_f32_e32 v68, v68, v99
	ds_bpermute_b32 v69, v29, v68
	s_waitcnt lgkmcnt(0)
	v_add_f32_e32 v68, v68, v69
	ds_bpermute_b32 v69, v72, v68
	s_waitcnt lgkmcnt(0)
	v_add_f32_e32 v68, v68, v69
	ds_bpermute_b32 v69, v73, v68
	s_waitcnt lgkmcnt(0)
	v_add_f32_e32 v68, v68, v69
	ds_bpermute_b32 v69, v74, v68
	s_waitcnt lgkmcnt(0)
	v_add_f32_e32 v68, v68, v69
	ds_bpermute_b32 v69, v75, v68
	s_waitcnt lgkmcnt(0)
	v_add_f32_e32 v68, v68, v69
	ds_bpermute_b32 v69, v76, v68
	s_waitcnt lgkmcnt(0)
	v_add_f32_e32 v68, v68, v69
	v_fmamk_f32 v68, v68, 0x3a800000, v80
	v_mul_f32_e32 v69, 0x4b800000, v68
	v_cmp_gt_f32_e32 vcc, s40, v68
	s_nop 1
	v_cndmask_b32_e32 v68, v68, v69, vcc
	v_rsq_f32_e32 v68, v68
	s_nop 0
	v_mul_f32_e32 v69, 0x45800000, v68
	v_cndmask_b32_e32 v68, v68, v69, vcc
	v_pk_mul_f32 v[82:83], v[82:83], v[68:69] op_sel_hi:[1,0]
	v_pk_mul_f32 v[86:87], v[86:87], v[68:69] op_sel_hi:[1,0]
	v_pk_fma_f32 v[82:83], v[54:55], v[82:83], v[0:1]
	v_pk_mul_f32 v[92:93], v[92:93], v[68:69] op_sel_hi:[1,0]
	v_pk_fma_f32 v[86:87], v[58:59], v[86:87], v[4:5]
	v_mul_f32_e32 v82, 0x41800000, v82
	v_mul_f32_e32 v83, 0x41800000, v83
	v_pk_mul_f32 v[96:97], v[96:97], v[68:69] op_sel_hi:[1,0]
	v_pk_fma_f32 v[92:93], v[62:63], v[92:93], v[8:9]
	v_mul_f32_e32 v86, 0x41800000, v86
	v_mul_f32_e32 v87, 0x41800000, v87
	v_med3_f32 v82, v82, s41, v81
	v_med3_f32 v83, v83, s41, v81
	v_pk_mul_f32 v[84:85], v[84:85], v[68:69] op_sel_hi:[1,0]
	v_pk_mul_f32 v[88:89], v[88:89], v[68:69] op_sel_hi:[1,0]
	v_pk_mul_f32 v[90:91], v[90:91], v[68:69] op_sel_hi:[1,0]
	v_pk_mul_f32 v[68:69], v[94:95], v[68:69] op_sel_hi:[1,0]
	v_pk_fma_f32 v[94:95], v[66:67], v[96:97], v[12:13]
	v_mul_f32_e32 v92, 0x41800000, v92
	v_mul_f32_e32 v93, 0x41800000, v93
	v_med3_f32 v86, v86, s41, v81
	v_med3_f32 v87, v87, s41, v81
	v_cvt_pk_fp8_f32 v162, v82, v83
	v_pk_fma_f32 v[84:85], v[52:53], v[84:85], v[2:3]
	v_mul_f32_e32 v94, 0x41800000, v94
	v_mul_f32_e32 v95, 0x41800000, v95
	v_med3_f32 v92, v92, s41, v81
	v_med3_f32 v93, v93, s41, v81
	v_cvt_pk_fp8_f32 v163, v86, v87
	v_pk_fma_f32 v[88:89], v[56:57], v[88:89], v[6:7]
	v_mul_f32_e32 v84, 0x41800000, v84
	v_mul_f32_e32 v85, 0x41800000, v85
	v_med3_f32 v94, v94, s41, v81
	v_med3_f32 v95, v95, s41, v81
	v_cvt_pk_fp8_f32 v164, v92, v93
	v_pk_fma_f32 v[90:91], v[60:61], v[90:91], v[10:11]
	v_mul_f32_e32 v88, 0x41800000, v88
	v_mul_f32_e32 v89, 0x41800000, v89
	v_med3_f32 v84, v84, s41, v81
	v_med3_f32 v85, v85, s41, v81
	v_cvt_pk_fp8_f32 v165, v94, v95
	v_pk_fma_f32 v[68:69], v[64:65], v[68:69], v[14:15]
	v_mul_f32_e32 v90, 0x41800000, v90
	v_mul_f32_e32 v91, 0x41800000, v91
	v_med3_f32 v88, v88, s41, v81
	v_med3_f32 v89, v89, s41, v81
	v_cvt_pk_fp8_f32 v162, v84, v85 op_sel:[0,0,1]
	v_mul_f32_e32 v68, 0x41800000, v68
	v_mul_f32_e32 v69, 0x41800000, v69
	v_med3_f32 v90, v90, s41, v81
	v_med3_f32 v91, v91, s41, v81
	v_cvt_pk_fp8_f32 v163, v88, v89 op_sel:[0,0,1]
	v_med3_f32 v68, v68, s41, v81
	v_med3_f32 v69, v69, s41, v81
	v_cvt_pk_fp8_f32 v164, v90, v91 op_sel:[0,0,1]
	v_cvt_pk_fp8_f32 v165, v68, v69 op_sel:[0,0,1]
	global_store_dword v[70:71], v162, off
	global_store_dword v[70:71], v163, off offset:256
	global_store_dword v[70:71], v164, off offset:512
	global_store_dword v[70:71], v165, off offset:768
	s_cbranch_scc0 .LBB0_1602
	s_add_i32 s20, s20, s27
	s_add_i32 s33, s33, s36
	s_add_i32 s6, s6, s37
	s_cmpk_gt_i32 s20, 0x7ff
	s_cbranch_scc0 .LBB0_1601

; __device__ __forceinline__ void n1_phase(const Args& a, int layer, bool final_only, const int wv, const bool dry = false) {
;     ...
;     for (int run = F.bid * 8 + F.wave; run < NTOK / 16; run += F.G * 8) {
;         const int tok0 = run * 16, b = tok0 >> 12;
;         f32x4 g2s[4], ma[4], mb[4];
;         if (combine) { const float* g2 = mod + ((size_t)(layer - 1) * NBATCH + b) * 6144 + 5 * DM;
; #pragma unroll
;             for (int j = 0; j < 4; ++j) g2s[j] = *(const f32x4*)(g2 + 4 * F.lane + 256 * j) * (1.f / FP8_YSC); }
;         if (!final_only) { const float* sh = mod + ((size_t)layer * NBATCH + b) * 6144; const float* sc = sh + DM;
; #pragma unroll
;             for (int j = 0; j < 4; ++j) { const int c0 = 4 * F.lane + 256 * j; ma[j] = *(const f32x4*)(gmix + c0) * (*(const f32x4*)(sc + c0) + 1.f); mb[j] = *(const f32x4*)(sh + c0); } }
; #pragma unroll 1
;         for (int i = 0; i < 16; ++i) {
;             const int tok = tok0 + i;
;             f32x4 v[4];
;             if (layer == 0) ld_row16(a.x + (size_t)tok * DM, F.lane, v);
;             else {
; #pragma unroll
;                 for (int j = 0; j < 4; ++j) { const u32x2 w = *(const u32x2*)(XB + (size_t)tok * DM + 4 * F.lane + 256 * j); v[j] = (f32x4){bf_lo(w.x), bf_hi(w.x), bf_lo(w.y), bf_hi(w.y)}; } }
;             if (combine) {
;                 f32x4 ysum[4];
; #pragma unroll
;                 for (int j = 0; j < 4; ++j) ysum[j] = (f32x4){0.f, 0.f, 0.f, 0.f};
; #pragma unroll
;                 for (int k = 0; k < 4; ++k) { const int e = toke[tok * 4 + k], r = tokr[tok * 4 + k]; const size_t slot = (size_t)ps[e] + r;
.LBB0_4076:
	s_ashr_i32 s7, s6, 31
	s_lshl_b64 s[2:3], s[6:7], 10
	s_lshl_b64 s[16:17], s[6:7], 11
	s_ashr_i32 s7, s20, 8
	s_mul_hi_i32 s43, s7, 0x6000
	s_mulk_i32 s7, 0x6000
	s_add_u32 s44, s21, s7
	s_addc_u32 s45, s22, s43
	v_lshl_add_u64 v[0:1], s[44:45], 0, v[30:31]
	v_lshl_add_u64 v[2:3], v[0:1], 0, s[8:9]
	v_add_co_u32_e32 v0, vcc, s38, v0
	s_add_u32 s46, s44, 0x90000
	s_nop 0
	v_addc_co_u32_e32 v1, vcc, 0, v1, vcc
	global_load_dwordx4 v[38:41], v[0:1], off
	global_load_dwordx4 v[42:45], v[2:3], off offset:1024
	global_load_dwordx4 v[46:49], v[2:3], off offset:2048
	global_load_dwordx4 v[50:53], v[2:3], off offset:3072
	s_addc_u32 s47, s45, 0
	s_add_u32 s44, s44, 0x91000
	s_addc_u32 s45, s45, 0
	global_load_dwordx4 v[54:57], v30, s[44:45]
	global_load_dwordx4 v[58:61], v77, s[44:45]
	global_load_dwordx4 v[62:65], v78, s[44:45]
	global_load_dwordx4 v[66:69], v79, s[44:45]
	global_load_dwordx4 v[82:85], v[20:21], off
	global_load_dwordx4 v[86:89], v[22:23], off
	global_load_dwordx4 v[90:93], v[24:25], off
	global_load_dwordx4 v[0:3], v30, s[46:47]
	global_load_dwordx4 v[94:97], v[26:27], off
	global_load_dwordx4 v[4:7], v77, s[46:47]
	global_load_dwordx4 v[8:11], v78, s[46:47]
	global_load_dwordx4 v[12:15], v79, s[46:47]
	v_mov_b32_e32 v33, s3
	v_or_b32_e32 v32, s2, v16
	v_mov_b32_e32 v35, s17
	v_or_b32_e32 v34, s16, v28
	s_mov_b32 s7, 0
	s_waitcnt vmcnt(11)
	v_pk_add_f32 v[54:55], v[54:55], 1.0 op_sel_hi:[1,0]
	s_waitcnt vmcnt(10)
	v_pk_add_f32 v[58:59], v[58:59], 1.0 op_sel_hi:[1,0]
	s_waitcnt vmcnt(9)
	v_pk_add_f32 v[62:63], v[62:63], 1.0 op_sel_hi:[1,0]
	s_waitcnt vmcnt(8)
	v_pk_add_f32 v[66:67], v[66:67], 1.0 op_sel_hi:[1,0]
	v_pk_mul_f32 v[36:37], v[40:41], s[10:11] op_sel_hi:[1,0]
	v_pk_mul_f32 v[40:41], v[44:45], s[10:11] op_sel_hi:[1,0]
	v_pk_mul_f32 v[44:45], v[48:49], s[10:11] op_sel_hi:[1,0]
	v_pk_mul_f32 v[48:49], v[52:53], s[10:11] op_sel_hi:[1,0]
	v_pk_add_f32 v[52:53], v[56:57], 1.0 op_sel_hi:[1,0]
	v_pk_add_f32 v[56:57], v[60:61], 1.0 op_sel_hi:[1,0]
	v_pk_add_f32 v[60:61], v[64:65], 1.0 op_sel_hi:[1,0]
	v_pk_add_f32 v[64:65], v[68:69], 1.0 op_sel_hi:[1,0]
	v_pk_mul_f32 v[38:39], v[38:39], s[10:11] op_sel_hi:[1,0]
	v_pk_mul_f32 v[42:43], v[42:43], s[10:11] op_sel_hi:[1,0]
	v_pk_mul_f32 v[46:47], v[46:47], s[10:11] op_sel_hi:[1,0]
	v_pk_mul_f32 v[50:51], v[50:51], s[10:11] op_sel_hi:[1,0]
	s_waitcnt vmcnt(7)
	v_pk_mul_f32 v[52:53], v[84:85], v[52:53]
	v_pk_mul_f32 v[54:55], v[82:83], v[54:55]
	s_waitcnt vmcnt(6)
	v_pk_mul_f32 v[56:57], v[88:89], v[56:57]
	v_pk_mul_f32 v[58:59], v[86:87], v[58:59]
	s_waitcnt vmcnt(5)
	v_pk_mul_f32 v[60:61], v[92:93], v[60:61]
	v_pk_mul_f32 v[62:63], v[90:91], v[62:63]
	s_waitcnt vmcnt(3)
	v_pk_mul_f32 v[64:65], v[96:97], v[64:65]
	v_pk_mul_f32 v[66:67], v[94:95], v[66:67]
	v_lshl_add_u64 v[166:167], s[4:5], 0, v[34:35]
	s_add_i32 s16, s33, s7
	s_ashr_i32 s17, s16, 31
	s_lshl_b64 s[2:3], s[16:17], 2
	v_add_co_u32_e32 v166, vcc, 0xaf200000, v166
	s_add_u32 s44, s23, s2
	s_nop 0
	v_addc_co_u32_e32 v167, vcc, 0, v167, vcc
	s_addc_u32 s45, s24, s3
	global_load_dwordx2 v[170:171], v[166:167], off
	global_load_dwordx2 v[172:173], v[166:167], off offset:512
	global_load_dwordx2 v[174:175], v[166:167], off offset:1024
	global_load_dwordx2 v[176:177], v[166:167], off offset:1536
	global_load_dwordx4 v[178:181], v17, s[44:45]
	s_add_u32 s2, s25, s2
	s_addc_u32 s3, s26, s3
	s_add_i32 s16, s16, 1
	s_ashr_i32 s17, s16, 31
	global_load_dword v182, v17, s[2:3]
	s_lshl_b64 s[2:3], s[16:17], 2
	s_add_u32 s2, s25, s2
	s_addc_u32 s3, s26, s3
	global_load_dwordx3 v[184:186], v17, s[2:3]
	s_waitcnt vmcnt(0)
